# in-proj GEMM K-loops: the six LDS-DMA pieces of quarters 2 and 4 issued between that quarter's MFMAs instead of before its first barrier (vmcnt 8 -> 2 there)
# speedup vs baseline: 1.0068x; 1.0027x over previous
.LBB0_124:
	s_add_i32 s79, s56, 2
	s_add_u32 s58, s54, 0x80
	s_addc_u32 s57, s55, 0
	s_cmp_eq_u32 s70, s56
	s_cselect_b32 s57, s41, s57
	s_cselect_b32 s56, s40, s58
	s_cselect_b32 s59, s53, s78
	s_cselect_b32 s58, s52, s77
	s_add_i32 s80, 0, 0x10000
	s_add_i32 s81, 0, 0x14000
	v_add_u32_e32 v2, s80, v183
	v_add_u32_e32 v14, s81, v183
	ds_read_b128 v[18:21], v2
	ds_read_b128 v[22:25], v2 offset:1024
	ds_read_b128 v[26:29], v2 offset:2048
	ds_read_b128 v[30:33], v2 offset:3072
	ds_read_b128 v[2:5], v14
	ds_read_b128 v[6:9], v14 offset:1024
	ds_read_b128 v[10:13], v14 offset:2048
	ds_read_b128 v[14:17], v14 offset:3072
	v_lshl_add_u64 v[176:177], s[54:55], 0, v[164:165]
	s_add_i32 m0, s62, 0xc000
	ds_read_b128 v[168:171], v184
	ds_read_b128 v[172:175], v184 offset:1024
	ds_read_b128 v[186:189], v184 offset:2048
	ds_read_b128 v[190:193], v184 offset:3072
	ds_read_b128 v[194:197], v184 offset:4096
	ds_read_b128 v[198:201], v184 offset:5120
	ds_read_b128 v[202:205], v184 offset:6144
	ds_read_b128 v[206:209], v184 offset:7168
	global_load_lds_dwordx4 v[176:177], off
	v_lshl_add_u64 v[176:177], s[54:55], 0, v[166:167]
	s_add_i32 m0, s62, 0xe000
	s_nop 0
	global_load_lds_dwordx4 v[176:177], off
	s_waitcnt vmcnt(8)
	s_waitcnt lgkmcnt(0)
	s_barrier
	s_setprio 1
	s_waitcnt lgkmcnt(0)
	v_mfma_scale_f32_16x16x128_f8f6f4 v[154:157], v[18:25], v[168:175], v[154:157], v180, v180 op_sel_hi:[0,0,0]
	v_mfma_scale_f32_16x16x128_f8f6f4 v[158:161], v[26:33], v[168:175], v[158:161], v180, v180 op_sel_hi:[0,0,0]
	v_mfma_scale_f32_16x16x128_f8f6f4 v[142:145], v[18:25], v[186:193], v[142:145], v180, v180 op_sel_hi:[0,0,0]
	v_mfma_scale_f32_16x16x128_f8f6f4 v[138:141], v[26:33], v[186:193], v[138:141], v180, v180 op_sel_hi:[0,0,0]
	v_mfma_scale_f32_16x16x128_f8f6f4 v[126:129], v[18:25], v[194:201], v[126:129], v180, v180 op_sel_hi:[0,0,0]
	v_mfma_scale_f32_16x16x128_f8f6f4 v[122:125], v[26:33], v[194:201], v[122:125], v180, v180 op_sel_hi:[0,0,0]
	v_mfma_scale_f32_16x16x128_f8f6f4 v[110:113], v[18:25], v[202:209], v[110:113], v180, v180 op_sel_hi:[0,0,0]
	v_mfma_scale_f32_16x16x128_f8f6f4 v[106:109], v[26:33], v[202:209], v[106:109], v180, v180 op_sel_hi:[0,0,0]
	s_setprio 0
	s_setprio 1
	v_mfma_scale_f32_16x16x128_f8f6f4 v[150:153], v[2:9], v[168:175], v[150:153], v180, v180 op_sel_hi:[0,0,0]
	v_mfma_scale_f32_16x16x128_f8f6f4 v[146:149], v[10:17], v[168:175], v[146:149], v180, v180 op_sel_hi:[0,0,0]
	v_mfma_scale_f32_16x16x128_f8f6f4 v[134:137], v[2:9], v[186:193], v[134:137], v180, v180 op_sel_hi:[0,0,0]
	v_mfma_scale_f32_16x16x128_f8f6f4 v[130:133], v[10:17], v[186:193], v[130:133], v180, v180 op_sel_hi:[0,0,0]
	v_mfma_scale_f32_16x16x128_f8f6f4 v[118:121], v[2:9], v[194:201], v[118:121], v180, v180 op_sel_hi:[0,0,0]
	v_mfma_scale_f32_16x16x128_f8f6f4 v[114:117], v[10:17], v[194:201], v[114:117], v180, v180 op_sel_hi:[0,0,0]
	v_mfma_scale_f32_16x16x128_f8f6f4 v[102:105], v[2:9], v[202:209], v[102:105], v180, v180 op_sel_hi:[0,0,0]
	v_mfma_scale_f32_16x16x128_f8f6f4 v[98:101], v[10:17], v[202:209], v[98:101], v180, v180 op_sel_hi:[0,0,0]
	s_setprio 0
	s_barrier
	ds_read_b128 v[186:189], v184 offset:16384
	ds_read_b128 v[190:193], v184 offset:17408
	ds_read_b128 v[194:197], v184 offset:18432
	ds_read_b128 v[198:201], v184 offset:19456
	ds_read_b128 v[202:205], v184 offset:20480
	ds_read_b128 v[206:209], v184 offset:21504
	ds_read_b128 v[212:215], v184 offset:22528
	ds_read_b128 v[216:219], v184 offset:23552
	s_waitcnt vmcnt(2)
	s_waitcnt lgkmcnt(0)
	s_barrier
	s_setprio 1
	s_waitcnt lgkmcnt(0)
	v_mfma_scale_f32_16x16x128_f8f6f4 v[94:97], v[18:25], v[186:193], v[94:97], v180, v180 op_sel_hi:[0,0,0]
	s_add_i32 s80, s80, s20
	v_lshl_add_u64 v[168:169], s[58:59], 0, v[0:1]
	s_mov_b32 m0, s80
	v_mfma_scale_f32_16x16x128_f8f6f4 v[90:93], v[26:33], v[186:193], v[90:93], v180, v180 op_sel_hi:[0,0,0]
	global_load_lds_dwordx4 v[168:169], off
	v_mfma_scale_f32_16x16x128_f8f6f4 v[78:81], v[18:25], v[194:201], v[78:81], v180, v180 op_sel_hi:[0,0,0]
	s_add_i32 m0, s80, 0x2000
	s_add_u32 s58, s58, s8
	s_addc_u32 s59, s59, s9
	v_lshl_add_u64 v[170:171], v[168:169], 0, s[6:7]
	v_lshl_add_u64 v[172:173], s[58:59], 0, v[0:1]
	s_add_i32 s58, s81, s20
	v_mfma_scale_f32_16x16x128_f8f6f4 v[74:77], v[26:33], v[194:201], v[74:77], v180, v180 op_sel_hi:[0,0,0]
	global_load_lds_dwordx4 v[170:171], off
	v_mfma_scale_f32_16x16x128_f8f6f4 v[62:65], v[18:25], v[202:209], v[62:65], v180, v180 op_sel_hi:[0,0,0]
	s_mov_b32 m0, s58
	v_lshl_add_u64 v[174:175], v[172:173], 0, s[6:7]
	v_mfma_scale_f32_16x16x128_f8f6f4 v[58:61], v[26:33], v[202:209], v[58:61], v180, v180 op_sel_hi:[0,0,0]
	global_load_lds_dwordx4 v[172:173], off
	v_mfma_scale_f32_16x16x128_f8f6f4 v[46:49], v[18:25], v[212:219], v[46:49], v180, v180 op_sel_hi:[0,0,0]
	s_add_i32 m0, s58, 0x2000
	v_lshl_add_u64 v[176:177], s[56:57], 0, v[162:163]
	v_mfma_scale_f32_16x16x128_f8f6f4 v[42:45], v[26:33], v[212:219], v[42:45], v180, v180 op_sel_hi:[0,0,0]
	global_load_lds_dwordx4 v[174:175], off
	s_setprio 0
	s_setprio 1
	v_mfma_scale_f32_16x16x128_f8f6f4 v[86:89], v[2:9], v[186:193], v[86:89], v180, v180 op_sel_hi:[0,0,0]
	s_mov_b32 m0, s62
	v_lshl_add_u64 v[178:179], v[176:177], 0, s[6:7]
	v_mfma_scale_f32_16x16x128_f8f6f4 v[82:85], v[10:17], v[186:193], v[82:85], v180, v180 op_sel_hi:[0,0,0]
	global_load_lds_dwordx4 v[176:177], off
	v_mfma_scale_f32_16x16x128_f8f6f4 v[70:73], v[2:9], v[194:201], v[70:73], v180, v180 op_sel_hi:[0,0,0]
	s_mov_b32 m0, s63
	s_nop 0
	v_mfma_scale_f32_16x16x128_f8f6f4 v[66:69], v[10:17], v[194:201], v[66:69], v180, v180 op_sel_hi:[0,0,0]
	global_load_lds_dwordx4 v[178:179], off
	v_mfma_scale_f32_16x16x128_f8f6f4 v[54:57], v[2:9], v[202:209], v[54:57], v180, v180 op_sel_hi:[0,0,0]
	v_mfma_scale_f32_16x16x128_f8f6f4 v[50:53], v[10:17], v[202:209], v[50:53], v180, v180 op_sel_hi:[0,0,0]
	v_mfma_scale_f32_16x16x128_f8f6f4 v[38:41], v[2:9], v[212:219], v[38:41], v180, v180 op_sel_hi:[0,0,0]
	v_mfma_scale_f32_16x16x128_f8f6f4 v[34:37], v[10:17], v[212:219], v[34:37], v180, v180 op_sel_hi:[0,0,0]
	s_setprio 0
	s_barrier
	s_add_i32 s58, 0, 0x18000
	s_add_i32 s59, 0, 0x1c000
	v_add_u32_e32 v14, s58, v183
	v_add_u32_e32 v30, s59, v183
	ds_read_b128 v[2:5], v14
	ds_read_b128 v[6:9], v14 offset:1024
	ds_read_b128 v[10:13], v14 offset:2048
	ds_read_b128 v[14:17], v14 offset:3072
	ds_read_b128 v[18:21], v30
	ds_read_b128 v[22:25], v30 offset:1024
	ds_read_b128 v[26:29], v30 offset:2048
	ds_read_b128 v[30:33], v30 offset:3072
	s_add_u32 s56, s56, s8
	s_addc_u32 s57, s57, s9
	s_mov_b32 m0, s64
	v_lshl_add_u64 v[220:221], s[56:57], 0, v[162:163]
	ds_read_b128 v[186:189], v184 offset:32768
	ds_read_b128 v[190:193], v184 offset:33792
	ds_read_b128 v[194:197], v184 offset:34816
	ds_read_b128 v[198:201], v184 offset:35840
	ds_read_b128 v[202:205], v184 offset:36864
	ds_read_b128 v[206:209], v184 offset:37888
	ds_read_b128 v[212:215], v184 offset:38912
	ds_read_b128 v[216:219], v184 offset:39936
	global_load_lds_dwordx4 v[220:221], off
	v_lshl_add_u64 v[220:221], v[220:221], 0, s[6:7]
	s_mov_b32 m0, s65
	s_nop 0
	global_load_lds_dwordx4 v[220:221], off
	s_waitcnt vmcnt(8)
	s_waitcnt lgkmcnt(0)
	s_barrier
	s_setprio 1
	s_waitcnt lgkmcnt(0)
	v_mfma_scale_f32_16x16x128_f8f6f4 v[154:157], v[2:9], v[186:193], v[154:157], v180, v180 op_sel_hi:[0,0,0]
	v_mfma_scale_f32_16x16x128_f8f6f4 v[158:161], v[10:17], v[186:193], v[158:161], v180, v180 op_sel_hi:[0,0,0]
	v_mfma_scale_f32_16x16x128_f8f6f4 v[142:145], v[2:9], v[194:201], v[142:145], v180, v180 op_sel_hi:[0,0,0]
	v_mfma_scale_f32_16x16x128_f8f6f4 v[138:141], v[10:17], v[194:201], v[138:141], v180, v180 op_sel_hi:[0,0,0]
	v_mfma_scale_f32_16x16x128_f8f6f4 v[126:129], v[2:9], v[202:209], v[126:129], v180, v180 op_sel_hi:[0,0,0]
	v_mfma_scale_f32_16x16x128_f8f6f4 v[122:125], v[10:17], v[202:209], v[122:125], v180, v180 op_sel_hi:[0,0,0]
	v_mfma_scale_f32_16x16x128_f8f6f4 v[110:113], v[2:9], v[212:219], v[110:113], v180, v180 op_sel_hi:[0,0,0]
	v_mfma_scale_f32_16x16x128_f8f6f4 v[106:109], v[10:17], v[212:219], v[106:109], v180, v180 op_sel_hi:[0,0,0]
	s_setprio 0
	s_setprio 1
	v_mfma_scale_f32_16x16x128_f8f6f4 v[150:153], v[18:25], v[186:193], v[150:153], v180, v180 op_sel_hi:[0,0,0]
	v_mfma_scale_f32_16x16x128_f8f6f4 v[146:149], v[26:33], v[186:193], v[146:149], v180, v180 op_sel_hi:[0,0,0]
	v_mfma_scale_f32_16x16x128_f8f6f4 v[134:137], v[18:25], v[194:201], v[134:137], v180, v180 op_sel_hi:[0,0,0]
	v_mfma_scale_f32_16x16x128_f8f6f4 v[130:133], v[26:33], v[194:201], v[130:133], v180, v180 op_sel_hi:[0,0,0]
	v_mfma_scale_f32_16x16x128_f8f6f4 v[118:121], v[18:25], v[202:209], v[118:121], v180, v180 op_sel_hi:[0,0,0]
	v_mfma_scale_f32_16x16x128_f8f6f4 v[114:117], v[26:33], v[202:209], v[114:117], v180, v180 op_sel_hi:[0,0,0]
	v_mfma_scale_f32_16x16x128_f8f6f4 v[102:105], v[18:25], v[212:219], v[102:105], v180, v180 op_sel_hi:[0,0,0]
	v_mfma_scale_f32_16x16x128_f8f6f4 v[98:101], v[26:33], v[212:219], v[98:101], v180, v180 op_sel_hi:[0,0,0]
	s_setprio 0
	s_barrier
	ds_read_b128 v[186:189], v184 offset:49152
	ds_read_b128 v[190:193], v184 offset:50176
	ds_read_b128 v[194:197], v184 offset:51200
	ds_read_b128 v[198:201], v184 offset:52224
	ds_read_b128 v[202:205], v184 offset:53248
	ds_read_b128 v[206:209], v184 offset:54272
	ds_read_b128 v[212:215], v184 offset:55296
	ds_read_b128 v[216:219], v184 offset:56320
	s_waitcnt vmcnt(2)
	s_waitcnt lgkmcnt(0)
	s_barrier
	s_setprio 1
	s_waitcnt lgkmcnt(0)
	v_mfma_scale_f32_16x16x128_f8f6f4 v[94:97], v[2:9], v[186:193], v[94:97], v180, v180 op_sel_hi:[0,0,0]
	s_add_i32 s56, s58, s20
	v_lshl_add_u64 v[168:169], v[168:169], 0, s[36:37]
	s_mov_b32 m0, s56
	v_mfma_scale_f32_16x16x128_f8f6f4 v[90:93], v[10:17], v[186:193], v[90:93], v180, v180 op_sel_hi:[0,0,0]
	global_load_lds_dwordx4 v[168:169], off
	v_mfma_scale_f32_16x16x128_f8f6f4 v[78:81], v[2:9], v[194:201], v[78:81], v180, v180 op_sel_hi:[0,0,0]
	v_lshl_add_u64 v[168:169], v[170:171], 0, s[36:37]
	s_add_i32 m0, s56, 0x2000
	s_add_i32 s56, s59, s20
	v_mfma_scale_f32_16x16x128_f8f6f4 v[74:77], v[10:17], v[194:201], v[74:77], v180, v180 op_sel_hi:[0,0,0]
	global_load_lds_dwordx4 v[168:169], off
	v_mfma_scale_f32_16x16x128_f8f6f4 v[62:65], v[2:9], v[202:209], v[62:65], v180, v180 op_sel_hi:[0,0,0]
	v_lshl_add_u64 v[168:169], v[172:173], 0, s[36:37]
	s_mov_b32 m0, s56
	s_nop 0
	v_mfma_scale_f32_16x16x128_f8f6f4 v[58:61], v[10:17], v[202:209], v[58:61], v180, v180 op_sel_hi:[0,0,0]
	global_load_lds_dwordx4 v[168:169], off
	v_mfma_scale_f32_16x16x128_f8f6f4 v[46:49], v[2:9], v[212:219], v[46:49], v180, v180 op_sel_hi:[0,0,0]
	v_lshl_add_u64 v[168:169], v[174:175], 0, s[36:37]
	s_add_i32 m0, s56, 0x2000
	s_nop 0
	v_mfma_scale_f32_16x16x128_f8f6f4 v[42:45], v[10:17], v[212:219], v[42:45], v180, v180 op_sel_hi:[0,0,0]
	global_load_lds_dwordx4 v[168:169], off
	s_setprio 0
	s_setprio 1
	v_mfma_scale_f32_16x16x128_f8f6f4 v[86:89], v[18:25], v[186:193], v[86:89], v180, v180 op_sel_hi:[0,0,0]
	v_lshl_add_u64 v[168:169], v[176:177], 0, s[36:37]
	s_mov_b32 m0, s66
	s_nop 0
	v_mfma_scale_f32_16x16x128_f8f6f4 v[82:85], v[26:33], v[186:193], v[82:85], v180, v180 op_sel_hi:[0,0,0]
	global_load_lds_dwordx4 v[168:169], off
	v_mfma_scale_f32_16x16x128_f8f6f4 v[70:73], v[18:25], v[194:201], v[70:73], v180, v180 op_sel_hi:[0,0,0]
	v_lshl_add_u64 v[168:169], v[178:179], 0, s[36:37]
	s_mov_b32 m0, s67
	s_nop 0
	v_mfma_scale_f32_16x16x128_f8f6f4 v[66:69], v[26:33], v[194:201], v[66:69], v180, v180 op_sel_hi:[0,0,0]
	global_load_lds_dwordx4 v[168:169], off
	v_mfma_scale_f32_16x16x128_f8f6f4 v[54:57], v[18:25], v[202:209], v[54:57], v180, v180 op_sel_hi:[0,0,0]
	v_mfma_scale_f32_16x16x128_f8f6f4 v[50:53], v[26:33], v[202:209], v[50:53], v180, v180 op_sel_hi:[0,0,0]
	v_mfma_scale_f32_16x16x128_f8f6f4 v[38:41], v[18:25], v[212:219], v[38:41], v180, v180 op_sel_hi:[0,0,0]
	v_mfma_scale_f32_16x16x128_f8f6f4 v[34:37], v[26:33], v[212:219], v[34:37], v180, v180 op_sel_hi:[0,0,0]
	s_setprio 0
	s_barrier
	s_add_u32 s54, s54, 0x100
	s_addc_u32 s55, s55, 0
	s_add_u32 s77, s77, 0x100
	s_addc_u32 s78, s78, 0
	s_cmp_ge_i32 s79, s30
	s_mov_b32 s56, s79
	s_cbranch_scc0 .LBB0_124

.LBB0_145:
	s_add_i32 s79, s56, 2
	s_add_u32 s58, s54, 0x80
	s_addc_u32 s57, s55, 0
	s_cmp_eq_u32 s73, s56
	s_cselect_b32 s57, s41, s57
	s_cselect_b32 s56, s40, s58
	s_cselect_b32 s59, s53, s78
	s_cselect_b32 s58, s52, s70
	s_add_i32 s80, 0, 0x10000
	s_add_i32 s81, 0, 0x14000
	v_add_u32_e32 v2, s80, v182
	v_add_u32_e32 v14, s81, v182
	ds_read_b128 v[18:21], v2
	ds_read_b128 v[22:25], v2 offset:1024
	ds_read_b128 v[26:29], v2 offset:2048
	ds_read_b128 v[30:33], v2 offset:3072
	ds_read_b128 v[2:5], v14
	ds_read_b128 v[6:9], v14 offset:1024
	ds_read_b128 v[10:13], v14 offset:2048
	ds_read_b128 v[14:17], v14 offset:3072
	v_lshl_add_u64 v[176:177], s[54:55], 0, v[164:165]
	s_add_i32 m0, s64, 0xc000
	ds_read_b128 v[168:171], v183
	ds_read_b128 v[172:175], v183 offset:1024
	ds_read_b128 v[184:187], v183 offset:2048
	ds_read_b128 v[188:191], v183 offset:3072
	ds_read_b128 v[192:195], v183 offset:4096
	ds_read_b128 v[196:199], v183 offset:5120
	ds_read_b128 v[200:203], v183 offset:6144
	ds_read_b128 v[204:207], v183 offset:7168
	global_load_lds_dwordx4 v[176:177], off
	v_lshl_add_u64 v[176:177], s[54:55], 0, v[166:167]
	s_add_i32 m0, s64, 0xe000
	s_nop 0
	global_load_lds_dwordx4 v[176:177], off
	s_waitcnt vmcnt(8)
	s_waitcnt lgkmcnt(0)
	s_barrier
	s_setprio 1
	s_waitcnt lgkmcnt(0)
	v_mfma_scale_f32_16x16x128_f8f6f4 v[158:161], v[18:25], v[168:175], v[158:161], v180, v180 op_sel_hi:[0,0,0]
	v_mfma_scale_f32_16x16x128_f8f6f4 v[154:157], v[26:33], v[168:175], v[154:157], v180, v180 op_sel_hi:[0,0,0]
	v_mfma_scale_f32_16x16x128_f8f6f4 v[142:145], v[18:25], v[184:191], v[142:145], v180, v180 op_sel_hi:[0,0,0]
	v_mfma_scale_f32_16x16x128_f8f6f4 v[138:141], v[26:33], v[184:191], v[138:141], v180, v180 op_sel_hi:[0,0,0]
	v_mfma_scale_f32_16x16x128_f8f6f4 v[126:129], v[18:25], v[192:199], v[126:129], v180, v180 op_sel_hi:[0,0,0]
	v_mfma_scale_f32_16x16x128_f8f6f4 v[122:125], v[26:33], v[192:199], v[122:125], v180, v180 op_sel_hi:[0,0,0]
	v_mfma_scale_f32_16x16x128_f8f6f4 v[110:113], v[18:25], v[200:207], v[110:113], v180, v180 op_sel_hi:[0,0,0]
	v_mfma_scale_f32_16x16x128_f8f6f4 v[106:109], v[26:33], v[200:207], v[106:109], v180, v180 op_sel_hi:[0,0,0]
	s_setprio 0
	s_setprio 1
	v_mfma_scale_f32_16x16x128_f8f6f4 v[150:153], v[2:9], v[168:175], v[150:153], v180, v180 op_sel_hi:[0,0,0]
	v_mfma_scale_f32_16x16x128_f8f6f4 v[146:149], v[10:17], v[168:175], v[146:149], v180, v180 op_sel_hi:[0,0,0]
	v_mfma_scale_f32_16x16x128_f8f6f4 v[134:137], v[2:9], v[184:191], v[134:137], v180, v180 op_sel_hi:[0,0,0]
	v_mfma_scale_f32_16x16x128_f8f6f4 v[130:133], v[10:17], v[184:191], v[130:133], v180, v180 op_sel_hi:[0,0,0]
	v_mfma_scale_f32_16x16x128_f8f6f4 v[118:121], v[2:9], v[192:199], v[118:121], v180, v180 op_sel_hi:[0,0,0]
	v_mfma_scale_f32_16x16x128_f8f6f4 v[114:117], v[10:17], v[192:199], v[114:117], v180, v180 op_sel_hi:[0,0,0]
	v_mfma_scale_f32_16x16x128_f8f6f4 v[102:105], v[2:9], v[200:207], v[102:105], v180, v180 op_sel_hi:[0,0,0]
	v_mfma_scale_f32_16x16x128_f8f6f4 v[98:101], v[10:17], v[200:207], v[98:101], v180, v180 op_sel_hi:[0,0,0]
	s_setprio 0
	s_barrier
	ds_read_b128 v[184:187], v183 offset:16384
	ds_read_b128 v[188:191], v183 offset:17408
	ds_read_b128 v[192:195], v183 offset:18432
	ds_read_b128 v[196:199], v183 offset:19456
	ds_read_b128 v[200:203], v183 offset:20480
	ds_read_b128 v[204:207], v183 offset:21504
	ds_read_b128 v[212:215], v183 offset:22528
	ds_read_b128 v[216:219], v183 offset:23552
	s_waitcnt vmcnt(2)
	s_waitcnt lgkmcnt(0)
	s_barrier
	s_setprio 1
	s_waitcnt lgkmcnt(0)
	v_mfma_scale_f32_16x16x128_f8f6f4 v[94:97], v[18:25], v[184:191], v[94:97], v180, v180 op_sel_hi:[0,0,0]
	s_add_i32 s80, s80, s62
	v_lshl_add_u64 v[168:169], s[58:59], 0, v[0:1]
	s_mov_b32 m0, s80
	v_mfma_scale_f32_16x16x128_f8f6f4 v[90:93], v[26:33], v[184:191], v[90:93], v180, v180 op_sel_hi:[0,0,0]
	global_load_lds_dwordx4 v[168:169], off
	v_mfma_scale_f32_16x16x128_f8f6f4 v[78:81], v[18:25], v[192:199], v[78:81], v180, v180 op_sel_hi:[0,0,0]
	s_add_i32 m0, s80, 0x2000
	s_add_u32 s58, s58, s8
	s_addc_u32 s59, s59, s9
	v_lshl_add_u64 v[170:171], v[168:169], 0, s[6:7]
	v_lshl_add_u64 v[172:173], s[58:59], 0, v[0:1]
	s_add_i32 s58, s81, s62
	v_mfma_scale_f32_16x16x128_f8f6f4 v[74:77], v[26:33], v[192:199], v[74:77], v180, v180 op_sel_hi:[0,0,0]
	global_load_lds_dwordx4 v[170:171], off
	v_mfma_scale_f32_16x16x128_f8f6f4 v[62:65], v[18:25], v[200:207], v[62:65], v180, v180 op_sel_hi:[0,0,0]
	s_mov_b32 m0, s58
	v_lshl_add_u64 v[174:175], v[172:173], 0, s[6:7]
	v_mfma_scale_f32_16x16x128_f8f6f4 v[58:61], v[26:33], v[200:207], v[58:61], v180, v180 op_sel_hi:[0,0,0]
	global_load_lds_dwordx4 v[172:173], off
	v_mfma_scale_f32_16x16x128_f8f6f4 v[46:49], v[18:25], v[212:219], v[46:49], v180, v180 op_sel_hi:[0,0,0]
	s_add_i32 m0, s58, 0x2000
	v_lshl_add_u64 v[176:177], s[56:57], 0, v[162:163]
	v_mfma_scale_f32_16x16x128_f8f6f4 v[42:45], v[26:33], v[212:219], v[42:45], v180, v180 op_sel_hi:[0,0,0]
	global_load_lds_dwordx4 v[174:175], off
	s_setprio 0
	s_setprio 1
	v_mfma_scale_f32_16x16x128_f8f6f4 v[86:89], v[2:9], v[184:191], v[86:89], v180, v180 op_sel_hi:[0,0,0]
	s_mov_b32 m0, s64
	v_lshl_add_u64 v[178:179], v[176:177], 0, s[10:11]
	v_mfma_scale_f32_16x16x128_f8f6f4 v[82:85], v[10:17], v[184:191], v[82:85], v180, v180 op_sel_hi:[0,0,0]
	global_load_lds_dwordx4 v[176:177], off
	v_mfma_scale_f32_16x16x128_f8f6f4 v[70:73], v[2:9], v[192:199], v[70:73], v180, v180 op_sel_hi:[0,0,0]
	s_mov_b32 m0, s65
	s_nop 0
	v_mfma_scale_f32_16x16x128_f8f6f4 v[66:69], v[10:17], v[192:199], v[66:69], v180, v180 op_sel_hi:[0,0,0]
	global_load_lds_dwordx4 v[178:179], off
	v_mfma_scale_f32_16x16x128_f8f6f4 v[54:57], v[2:9], v[200:207], v[54:57], v180, v180 op_sel_hi:[0,0,0]
	v_mfma_scale_f32_16x16x128_f8f6f4 v[50:53], v[10:17], v[200:207], v[50:53], v180, v180 op_sel_hi:[0,0,0]
	v_mfma_scale_f32_16x16x128_f8f6f4 v[38:41], v[2:9], v[212:219], v[38:41], v180, v180 op_sel_hi:[0,0,0]
	v_mfma_scale_f32_16x16x128_f8f6f4 v[34:37], v[10:17], v[212:219], v[34:37], v180, v180 op_sel_hi:[0,0,0]
	s_setprio 0
	s_barrier
	s_add_i32 s58, 0, 0x18000
	s_add_i32 s59, 0, 0x1c000
	v_add_u32_e32 v14, s58, v182
	v_add_u32_e32 v30, s59, v182
	ds_read_b128 v[2:5], v14
	ds_read_b128 v[6:9], v14 offset:1024
	ds_read_b128 v[10:13], v14 offset:2048
	ds_read_b128 v[14:17], v14 offset:3072
	ds_read_b128 v[18:21], v30
	ds_read_b128 v[22:25], v30 offset:1024
	ds_read_b128 v[26:29], v30 offset:2048
	ds_read_b128 v[30:33], v30 offset:3072
	s_add_u32 s56, s56, s6
	s_addc_u32 s57, s57, s7
	s_mov_b32 m0, s66
	v_lshl_add_u64 v[208:209], s[56:57], 0, v[162:163]
	ds_read_b128 v[184:187], v183 offset:32768
	ds_read_b128 v[188:191], v183 offset:33792
	ds_read_b128 v[192:195], v183 offset:34816
	ds_read_b128 v[196:199], v183 offset:35840
	ds_read_b128 v[200:203], v183 offset:36864
	ds_read_b128 v[204:207], v183 offset:37888
	ds_read_b128 v[212:215], v183 offset:38912
	ds_read_b128 v[216:219], v183 offset:39936
	global_load_lds_dwordx4 v[208:209], off
	v_lshl_add_u64 v[208:209], v[208:209], 0, s[10:11]
	s_mov_b32 m0, s67
	s_nop 0
	global_load_lds_dwordx4 v[208:209], off
	s_waitcnt vmcnt(8)
	s_waitcnt lgkmcnt(0)
	s_barrier
	s_setprio 1
	s_waitcnt lgkmcnt(0)
	v_mfma_scale_f32_16x16x128_f8f6f4 v[158:161], v[2:9], v[184:191], v[158:161], v180, v180 op_sel_hi:[0,0,0]
	v_mfma_scale_f32_16x16x128_f8f6f4 v[154:157], v[10:17], v[184:191], v[154:157], v180, v180 op_sel_hi:[0,0,0]
	v_mfma_scale_f32_16x16x128_f8f6f4 v[142:145], v[2:9], v[192:199], v[142:145], v180, v180 op_sel_hi:[0,0,0]
	v_mfma_scale_f32_16x16x128_f8f6f4 v[138:141], v[10:17], v[192:199], v[138:141], v180, v180 op_sel_hi:[0,0,0]
	v_mfma_scale_f32_16x16x128_f8f6f4 v[126:129], v[2:9], v[200:207], v[126:129], v180, v180 op_sel_hi:[0,0,0]
	v_mfma_scale_f32_16x16x128_f8f6f4 v[122:125], v[10:17], v[200:207], v[122:125], v180, v180 op_sel_hi:[0,0,0]
	v_mfma_scale_f32_16x16x128_f8f6f4 v[110:113], v[2:9], v[212:219], v[110:113], v180, v180 op_sel_hi:[0,0,0]
	v_mfma_scale_f32_16x16x128_f8f6f4 v[106:109], v[10:17], v[212:219], v[106:109], v180, v180 op_sel_hi:[0,0,0]
	s_setprio 0
	s_setprio 1
	v_mfma_scale_f32_16x16x128_f8f6f4 v[150:153], v[18:25], v[184:191], v[150:153], v180, v180 op_sel_hi:[0,0,0]
	v_mfma_scale_f32_16x16x128_f8f6f4 v[146:149], v[26:33], v[184:191], v[146:149], v180, v180 op_sel_hi:[0,0,0]
	v_mfma_scale_f32_16x16x128_f8f6f4 v[134:137], v[18:25], v[192:199], v[134:137], v180, v180 op_sel_hi:[0,0,0]
	v_mfma_scale_f32_16x16x128_f8f6f4 v[130:133], v[26:33], v[192:199], v[130:133], v180, v180 op_sel_hi:[0,0,0]
	v_mfma_scale_f32_16x16x128_f8f6f4 v[118:121], v[18:25], v[200:207], v[118:121], v180, v180 op_sel_hi:[0,0,0]
	v_mfma_scale_f32_16x16x128_f8f6f4 v[114:117], v[26:33], v[200:207], v[114:117], v180, v180 op_sel_hi:[0,0,0]
	v_mfma_scale_f32_16x16x128_f8f6f4 v[102:105], v[18:25], v[212:219], v[102:105], v180, v180 op_sel_hi:[0,0,0]
	v_mfma_scale_f32_16x16x128_f8f6f4 v[98:101], v[26:33], v[212:219], v[98:101], v180, v180 op_sel_hi:[0,0,0]
	s_setprio 0
	s_barrier
	ds_read_b128 v[184:187], v183 offset:49152
	ds_read_b128 v[188:191], v183 offset:50176
	ds_read_b128 v[192:195], v183 offset:51200
	ds_read_b128 v[196:199], v183 offset:52224
	ds_read_b128 v[200:203], v183 offset:53248
	ds_read_b128 v[204:207], v183 offset:54272
	ds_read_b128 v[212:215], v183 offset:55296
	ds_read_b128 v[216:219], v183 offset:56320
	s_waitcnt vmcnt(2)
	s_waitcnt lgkmcnt(0)
	s_barrier
	s_setprio 1
	s_waitcnt lgkmcnt(0)
	v_mfma_scale_f32_16x16x128_f8f6f4 v[94:97], v[2:9], v[184:191], v[94:97], v180, v180 op_sel_hi:[0,0,0]
	s_add_i32 s56, s58, s62
	v_lshl_add_u64 v[168:169], v[168:169], 0, s[36:37]
	s_mov_b32 m0, s56
	v_mfma_scale_f32_16x16x128_f8f6f4 v[90:93], v[10:17], v[184:191], v[90:93], v180, v180 op_sel_hi:[0,0,0]
	global_load_lds_dwordx4 v[168:169], off
	v_mfma_scale_f32_16x16x128_f8f6f4 v[78:81], v[2:9], v[192:199], v[78:81], v180, v180 op_sel_hi:[0,0,0]
	v_lshl_add_u64 v[168:169], v[170:171], 0, s[36:37]
	s_add_i32 m0, s56, 0x2000
	s_add_i32 s56, s59, s62
	v_mfma_scale_f32_16x16x128_f8f6f4 v[74:77], v[10:17], v[192:199], v[74:77], v180, v180 op_sel_hi:[0,0,0]
	global_load_lds_dwordx4 v[168:169], off
	v_mfma_scale_f32_16x16x128_f8f6f4 v[62:65], v[2:9], v[200:207], v[62:65], v180, v180 op_sel_hi:[0,0,0]
	v_lshl_add_u64 v[168:169], v[172:173], 0, s[36:37]
	s_mov_b32 m0, s56
	s_nop 0
	v_mfma_scale_f32_16x16x128_f8f6f4 v[58:61], v[10:17], v[200:207], v[58:61], v180, v180 op_sel_hi:[0,0,0]
	global_load_lds_dwordx4 v[168:169], off
	v_mfma_scale_f32_16x16x128_f8f6f4 v[46:49], v[2:9], v[212:219], v[46:49], v180, v180 op_sel_hi:[0,0,0]
	v_lshl_add_u64 v[168:169], v[174:175], 0, s[36:37]
	s_add_i32 m0, s56, 0x2000
	s_nop 0
	v_mfma_scale_f32_16x16x128_f8f6f4 v[42:45], v[10:17], v[212:219], v[42:45], v180, v180 op_sel_hi:[0,0,0]
	global_load_lds_dwordx4 v[168:169], off
	s_setprio 0
	s_setprio 1
	v_mfma_scale_f32_16x16x128_f8f6f4 v[86:89], v[18:25], v[184:191], v[86:89], v180, v180 op_sel_hi:[0,0,0]
	v_lshl_add_u64 v[168:169], v[176:177], 0, s[36:37]
	s_mov_b32 m0, s69
	s_nop 0
	v_mfma_scale_f32_16x16x128_f8f6f4 v[82:85], v[26:33], v[184:191], v[82:85], v180, v180 op_sel_hi:[0,0,0]
	global_load_lds_dwordx4 v[168:169], off
	v_mfma_scale_f32_16x16x128_f8f6f4 v[70:73], v[18:25], v[192:199], v[70:73], v180, v180 op_sel_hi:[0,0,0]
	v_lshl_add_u64 v[168:169], v[178:179], 0, s[36:37]
	s_mov_b32 m0, s72
	s_nop 0
	v_mfma_scale_f32_16x16x128_f8f6f4 v[66:69], v[26:33], v[192:199], v[66:69], v180, v180 op_sel_hi:[0,0,0]
	global_load_lds_dwordx4 v[168:169], off
	v_mfma_scale_f32_16x16x128_f8f6f4 v[54:57], v[18:25], v[200:207], v[54:57], v180, v180 op_sel_hi:[0,0,0]
	v_mfma_scale_f32_16x16x128_f8f6f4 v[50:53], v[26:33], v[200:207], v[50:53], v180, v180 op_sel_hi:[0,0,0]
	v_mfma_scale_f32_16x16x128_f8f6f4 v[38:41], v[18:25], v[212:219], v[38:41], v180, v180 op_sel_hi:[0,0,0]
	v_mfma_scale_f32_16x16x128_f8f6f4 v[34:37], v[26:33], v[212:219], v[34:37], v180, v180 op_sel_hi:[0,0,0]
	s_setprio 0
	s_barrier
	s_add_u32 s54, s54, 0x100
	s_addc_u32 s55, s55, 0
	s_add_u32 s70, s70, 0x100
	s_addc_u32 s78, s78, 0
	s_cmp_ge_i32 s79, s30
	s_mov_b32 s56, s79
	s_cbranch_scc0 .LBB0_145
	v_readlane_b32 s70, v254, 49
